# gen13 (staged last pass stored by waves 0-3 in their barrier wait) + sc0 nt policy on attn stores
# speedup vs baseline: 1.0252x; 1.0252x over previous
.LBB1_13:
	s_waitcnt vmcnt(12)
	v_cvt_pk_f16_f32 v151, v120, v121
	v_cvt_pk_f16_f32 v150, v100, v101
	v_cvt_pk_f16_f32 v149, v98, v99
	v_cvt_pk_f16_f32 v148, v112, v113
	s_add_i32 s24, s57, 1
	s_cmp_lg_u32 s57, 7
	s_waitcnt vmcnt(11)
	v_mfma_f32_32x32x16_f16 v[0:15], v[144:147], v[148:151], v[0:15]
	s_cselect_b32 s59, s24, 7
	s_lshl_b32 s25, s59, 2
	s_and_b32 s25, s25, 56
	s_or_b32 s58, s25, s27
	s_lshl_b32 s25, s55, 5
	s_and_b32 s59, s59, 1
	s_waitcnt vmcnt(10)
	v_mfma_f32_32x32x16_f16 v[16:31], v[140:143], v[148:151], v[16:31]
	v_cvt_pk_f16_f32 v143, v180, v181
	v_cvt_pk_f16_f32 v142, v124, v125
	v_cvt_pk_f16_f32 v141, v122, v123
	v_cvt_pk_f16_f32 v140, v102, v103
	s_waitcnt vmcnt(9)
	s_nop 0
	v_mfma_f32_32x32x16_f16 v[0:15], v[136:139], v[140:143], v[0:15]
	s_waitcnt vmcnt(8)
	v_mfma_f32_32x32x16_f16 v[16:31], v[132:135], v[140:143], v[16:31]
	s_add_i32 s61, s35, s60
	s_and_b32 s61, s61, 0x3f000
	v_or_b32_e32 v144, s61, v248
	s_add_i32 s61, s36, s60
	s_and_b32 s61, s61, 0x3f000
	v_or_b32_e32 v160, s61, v248
	global_load_dwordx4 v[132:135], v144, s[16:17]
	global_load_dwordx4 v[136:139], v144, s[16:17] offset:1024
	global_load_dwordx4 v[140:143], v144, s[16:17] offset:2048
	s_nop 0
	global_load_dwordx4 v[144:147], v144, s[16:17] offset:3072
	s_nop 0
	global_load_dwordx4 v[148:151], v160, s[16:17]
	global_load_dwordx4 v[152:155], v160, s[16:17] offset:1024
	global_load_dwordx4 v[156:159], v160, s[16:17] offset:2048
	s_nop 0
	global_load_dwordx4 v[160:163], v160, s[16:17] offset:3072
	v_cvt_pk_f16_f32 v253, v96, v97
	v_cvt_pk_f16_f32 v252, v84, v85
	v_cvt_pk_f16_f32 v251, v82, v83
	v_cvt_pk_f16_f32 v250, v80, v81
	s_waitcnt vmcnt(15)
	s_nop 0
	v_mfma_f32_32x32x16_f16 v[0:15], v[60:63], v[250:253], v[0:15]
	s_waitcnt vmcnt(14)
	v_mfma_f32_32x32x16_f16 v[16:31], v[56:59], v[250:253], v[16:31]
	v_cvt_pk_f16_f32 v59, v94, v95
	v_cvt_pk_f16_f32 v58, v90, v91
	v_cvt_pk_f16_f32 v57, v88, v89
	v_cvt_pk_f16_f32 v56, v86, v87
	s_waitcnt vmcnt(13)
	s_nop 0
	v_mfma_f32_32x32x16_f16 v[0:15], v[52:55], v[56:59], v[0:15]
	s_waitcnt vmcnt(12)
	v_mfma_f32_32x32x16_f16 v[16:31], v[48:51], v[56:59], v[16:31]
	v_cvt_pk_f16_f32 v51, v176, v177
	v_cvt_pk_f16_f32 v50, v110, v111
	v_cvt_pk_f16_f32 v49, v108, v109
	v_cvt_pk_f16_f32 v48, v92, v93
	s_waitcnt vmcnt(11)
	s_nop 0
	v_mfma_f32_32x32x16_f16 v[0:15], v[44:47], v[48:51], v[0:15]
	s_waitcnt vmcnt(10)
	v_mfma_f32_32x32x16_f16 v[16:31], v[40:43], v[48:51], v[16:31]
	v_cvt_pk_f16_f32 v43, v206, v207
	v_cvt_pk_f16_f32 v42, v194, v195
	v_cvt_pk_f16_f32 v41, v192, v193
	v_cvt_pk_f16_f32 v40, v174, v175
	s_waitcnt vmcnt(9)
	s_nop 0
	v_mfma_f32_32x32x16_f16 v[0:15], v[36:39], v[40:43], v[0:15]
	s_waitcnt vmcnt(8)
	v_mfma_f32_32x32x16_f16 v[16:31], v[32:35], v[40:43], v[16:31]
	s_add_i32 s61, s37, s60
	s_add_i32 s60, s38, s60
	s_and_b32 s61, s61, 0x3f000
	s_and_b32 s60, s60, 0x3f000
	v_or_b32_e32 v44, s61, v248
	v_or_b32_e32 v60, s60, v248
	global_load_dwordx4 v[32:35], v44, s[16:17]
	global_load_dwordx4 v[36:39], v44, s[16:17] offset:1024
	global_load_dwordx4 v[40:43], v44, s[16:17] offset:2048
	s_nop 0
	global_load_dwordx4 v[44:47], v44, s[16:17] offset:3072
	s_nop 0
	global_load_dwordx4 v[48:51], v60, s[16:17]
	global_load_dwordx4 v[52:55], v60, s[16:17] offset:1024
	global_load_dwordx4 v[56:59], v60, s[16:17] offset:2048
	s_nop 0
	global_load_dwordx4 v[60:63], v60, s[16:17] offset:3072
	v_cvt_pk_f16_f32 v251, v74, v75
	v_cvt_pk_f16_f32 v250, v68, v69
	v_cvt_pk_f16_f32 v249, v66, v67
	v_cvt_pk_f16_f32 v248, v64, v65
	s_waitcnt vmcnt(15)
	s_nop 0
	v_mfma_f32_32x32x16_f16 v[0:15], v[132:135], v[248:251], v[0:15]
	v_cvt_pk_f16_f32 v135, v172, v173
	v_cvt_pk_f16_f32 v134, v106, v107
	v_cvt_pk_f16_f32 v133, v104, v105
	v_cvt_pk_f16_f32 v132, v72, v73
	s_waitcnt vmcnt(14)
	v_mfma_f32_32x32x16_f16 v[16:31], v[136:139], v[248:251], v[16:31]
	s_waitcnt vmcnt(13)
	v_mfma_f32_32x32x16_f16 v[0:15], v[140:143], v[132:135], v[0:15]
	s_waitcnt vmcnt(12)
	v_mfma_f32_32x32x16_f16 v[16:31], v[144:147], v[132:135], v[16:31]
	v_cvt_pk_f16_f32 v135, v202, v203
	v_cvt_pk_f16_f32 v134, v190, v191
	v_cvt_pk_f16_f32 v133, v188, v189
	v_cvt_pk_f16_f32 v132, v170, v171
	s_waitcnt vmcnt(11)
	s_nop 0
	v_mfma_f32_32x32x16_f16 v[0:15], v[148:151], v[132:135], v[0:15]
	s_waitcnt vmcnt(10)
	v_mfma_f32_32x32x16_f16 v[16:31], v[152:155], v[132:135], v[16:31]
	v_cvt_pk_f16_f32 v135, v222, v223
	v_cvt_pk_f16_f32 v134, v216, v217
	v_cvt_pk_f16_f32 v133, v214, v215
	v_cvt_pk_f16_f32 v132, v200, v201
	s_waitcnt vmcnt(9)
	s_nop 0
	v_mfma_f32_32x32x16_f16 v[0:15], v[156:159], v[132:135], v[0:15]
	s_waitcnt vmcnt(8)
	v_mfma_f32_32x32x16_f16 v[16:31], v[160:163], v[132:135], v[16:31]
	v_cvt_pk_f16_f32 v135, v168, v169
	v_cvt_pk_f16_f32 v134, v78, v79
	v_cvt_pk_f16_f32 v133, v76, v77
	v_cvt_pk_f16_f32 v132, v70, v71
	s_waitcnt vmcnt(7)
	s_nop 0
	v_mfma_f32_32x32x16_f16 v[0:15], v[32:35], v[132:135], v[0:15]
	v_cvt_pk_f16_f32 v35, v198, v199
	v_cvt_pk_f16_f32 v34, v186, v187
	v_cvt_pk_f16_f32 v33, v184, v185
	v_cvt_pk_f16_f32 v32, v126, v127
	s_waitcnt vmcnt(6)
	v_mfma_f32_32x32x16_f16 v[16:31], v[36:39], v[132:135], v[16:31]
	s_waitcnt vmcnt(5)
	v_mfma_f32_32x32x16_f16 v[0:15], v[40:43], v[32:35], v[0:15]
	s_waitcnt vmcnt(4)
	v_mfma_f32_32x32x16_f16 v[16:31], v[44:47], v[32:35], v[16:31]
	v_cvt_pk_f16_f32 v35, v220, v221
	v_cvt_pk_f16_f32 v34, v212, v213
	v_cvt_pk_f16_f32 v33, v210, v211
	v_cvt_pk_f16_f32 v32, v196, v197
	s_waitcnt vmcnt(3)
	s_nop 0
	v_mfma_f32_32x32x16_f16 v[0:15], v[48:51], v[32:35], v[0:15]
	s_waitcnt vmcnt(2)
	v_mfma_f32_32x32x16_f16 v[16:31], v[52:55], v[32:35], v[16:31]
	v_cvt_pk_f16_f32 v35, v228, v229
	v_cvt_pk_f16_f32 v34, v226, v227
	v_cvt_pk_f16_f32 v33, v224, v225
	v_cvt_pk_f16_f32 v32, v218, v219
	s_waitcnt vmcnt(1)
	s_nop 0
	v_mfma_f32_32x32x16_f16 v[0:15], v[56:59], v[32:35], v[0:15]
	s_waitcnt vmcnt(0)
	v_mfma_f32_32x32x16_f16 v[16:31], v[60:63], v[32:35], v[16:31]
	s_cmp_lt_u32 s31, 0x200
	s_cbranch_scc0 .Lka_late
	s_or_b32 s62, s39, s59
	s_lshl_b32 s62, s62, 12
	s_lshl_b32 s66, s58, 18
	s_and_b32 s63, s62, 0x3f000
	s_or_b32 s63, s63, s66
	v_or_b32_e32 v252, s63, v231
	global_load_dwordx4 v[48:51], v252, s[6:7]
	global_load_dwordx4 v[52:55], v252, s[6:7] offset:1024
	global_load_dwordx4 v[56:59], v252, s[6:7] offset:2048
	global_load_dwordx4 v[60:63], v252, s[6:7] offset:3072
	s_add_i32 s63, s62, 0x4000
	s_and_b32 s63, s63, 0x3f000
	s_or_b32 s63, s63, s66
	v_or_b32_e32 v253, s63, v231
	global_load_dwordx4 v[40:43], v253, s[6:7] offset:2048
	global_load_dwordx4 v[44:47], v253, s[6:7] offset:3072
	s_add_i32 s63, s62, 0x6000
	s_and_b32 s63, s63, 0x3f000
	s_or_b32 s63, s63, s66
	v_or_b32_e32 v252, s63, v231
	global_load_dwordx4 v[148:151], v252, s[6:7] offset:3072
	s_add_i32 s63, s62, 0x7000
	s_and_b32 s63, s63, 0x3f000
	s_or_b32 s63, s63, s66
	v_or_b32_e32 v253, s63, v231
	global_load_dwordx4 v[132:135], v253, s[6:7]
	global_load_dwordx4 v[136:139], v253, s[6:7] offset:1024
	global_load_dwordx4 v[140:143], v253, s[6:7] offset:2048
	global_load_dwordx4 v[144:147], v253, s[6:7] offset:3072
	s_add_i32 s63, s62, 0x1000
	s_and_b32 s63, s63, 0x3f000
	s_or_b32 s63, s63, s66
	v_or_b32_e32 v252, s63, v231
	global_load_dwordx4 v[152:155], v252, s[6:7]
	global_load_dwordx4 v[156:159], v252, s[6:7] offset:1024
	s_cmp_eq_u32 s12, 0
	s_cbranch_scc1 .Lduty_done
	v_or_b32_e32 v252, s73, v239
	v_lshl_or_b32 v252, v252, 13, v240
	v_add_lshl_u32 v253, v241, s72, 7
	v_add_u32_e32 v253, 0x300, v253
	v_and_or_b32 v252, v253, s54, v252
	ds_read_b128 v[32:35], v246
	ds_read_b128 v[36:39], v246 offset:1088
	s_waitcnt lgkmcnt(1)
	global_store_dwordx4 v252, v[32:35], s[10:11] sc0 nt
	s_nop 0
	ds_read_b128 v[32:35], v246 offset:2176
	v_or_b32_e32 v253, 0x8000, v252
	s_waitcnt lgkmcnt(1)
	global_store_dwordx4 v253, v[36:39], s[10:11] sc0 nt
	s_nop 0
	ds_read_b128 v[36:39], v246 offset:3264
	v_or_b32_e32 v253, 0x10000, v252
	s_waitcnt lgkmcnt(1)
	global_store_dwordx4 v253, v[32:35], s[10:11] sc0 nt
	s_nop 0
	ds_read_b128 v[32:35], v246 offset:4352
	v_or_b32_e32 v253, 0x18000, v252
	s_waitcnt lgkmcnt(1)
	global_store_dwordx4 v253, v[36:39], s[10:11] sc0 nt
	s_nop 0
	ds_read_b128 v[36:39], v246 offset:5440
	v_or_b32_e32 v253, 0x20000, v252
	s_waitcnt lgkmcnt(1)
	global_store_dwordx4 v253, v[32:35], s[10:11] sc0 nt
	s_nop 0
	ds_read_b128 v[32:35], v246 offset:6528
	v_or_b32_e32 v253, 0x28000, v252
	s_waitcnt lgkmcnt(1)
	global_store_dwordx4 v253, v[36:39], s[10:11] sc0 nt
	s_nop 0
	ds_read_b128 v[36:39], v246 offset:7616
	v_or_b32_e32 v253, 0x30000, v252
	s_waitcnt lgkmcnt(1)
	global_store_dwordx4 v253, v[32:35], s[10:11] sc0 nt
	v_or_b32_e32 v253, 0x38000, v252
	s_waitcnt lgkmcnt(0)
	global_store_dwordx4 v253, v[36:39], s[10:11] sc0 nt
	v_mov_b32_e32 v252, s74
	s_movk_i32 s76, 0x1000

.Lduty_go:
	v_or_b32_e32 v252, s73, v239
	v_lshl_or_b32 v252, v252, 13, v240
	v_add_u32_e32 v253, 32, v241
	v_add_lshl_u32 v253, v253, s72, 7
	v_add_u32_e32 v253, 0x300, v253
	v_and_or_b32 v252, v253, s54, v252
	ds_read_b128 v[32:35], v246 offset:34816
	ds_read_b128 v[36:39], v246 offset:35904
	s_waitcnt lgkmcnt(1)
	global_store_dwordx4 v252, v[32:35], s[10:11] sc0 nt
	s_nop 0
	ds_read_b128 v[32:35], v246 offset:36992
	v_or_b32_e32 v253, 0x8000, v252
	s_waitcnt lgkmcnt(1)
	global_store_dwordx4 v253, v[36:39], s[10:11] sc0 nt
	s_nop 0
	ds_read_b128 v[36:39], v246 offset:38080
	v_or_b32_e32 v253, 0x10000, v252
	s_waitcnt lgkmcnt(1)
	global_store_dwordx4 v253, v[32:35], s[10:11] sc0 nt
	s_nop 0
	ds_read_b128 v[32:35], v246 offset:39168
	v_or_b32_e32 v253, 0x18000, v252
	s_waitcnt lgkmcnt(1)
	global_store_dwordx4 v253, v[36:39], s[10:11] sc0 nt
	s_nop 0
	ds_read_b128 v[36:39], v246 offset:40256
	v_or_b32_e32 v253, 0x20000, v252
	s_waitcnt lgkmcnt(1)
	global_store_dwordx4 v253, v[32:35], s[10:11] sc0 nt
	s_nop 0
	ds_read_b128 v[32:35], v246 offset:41344
	v_or_b32_e32 v253, 0x28000, v252
	s_waitcnt lgkmcnt(1)
	global_store_dwordx4 v253, v[36:39], s[10:11] sc0 nt
	s_nop 0
	ds_read_b128 v[36:39], v246 offset:42432
	v_or_b32_e32 v253, 0x30000, v252
	s_waitcnt lgkmcnt(1)
	global_store_dwordx4 v253, v[32:35], s[10:11] sc0 nt
	v_or_b32_e32 v253, 0x38000, v252
	s_waitcnt lgkmcnt(0)
	global_store_dwordx4 v253, v[36:39], s[10:11] sc0 nt

.Lka_done:
	ds_read2_b32 v[0:1], v235 offset1:32
	ds_read2_b32 v[2:3], v235 offset0:64 offset1:96
	ds_read2_b32 v[4:5], v235 offset0:128 offset1:160
	ds_read2_b32 v[6:7], v235 offset0:192 offset1:224
	ds_read2_b32 v[10:11], v236 offset0:128 offset1:160
	ds_read2_b32 v[16:17], v165 offset1:32
	ds_write_b128 v232, v[128:131]
	s_waitcnt lgkmcnt(6)
	v_max_f32_e32 v8, v1, v1
	v_max_f32_e32 v9, v0, v0
	v_max_f32_e32 v8, v9, v8
	s_waitcnt lgkmcnt(5)
	v_max3_f32 v8, v8, v2, v3
	s_waitcnt lgkmcnt(4)
	v_max3_f32 v8, v8, v4, v5
	s_waitcnt lgkmcnt(3)
	v_max3_f32 v14, v8, v6, v7
	ds_read2_b32 v[8:9], v236 offset1:32
	v_sub_f32_e32 v0, v0, v14
	v_sub_f32_e32 v1, v1, v14
	v_exp_f32_e32 v0, v0
	v_exp_f32_e32 v1, v1
	v_sub_f32_e32 v4, v4, v14
	v_sub_f32_e32 v5, v5, v14
	v_exp_f32_e32 v4, v4
	v_exp_f32_e32 v5, v5
	s_waitcnt lgkmcnt(0)
	v_pk_mul_f32 v[0:1], v[8:9], v[0:1]
	ds_read2_b32 v[8:9], v236 offset0:64 offset1:96
	v_sub_f32_e32 v2, v2, v14
	v_sub_f32_e32 v3, v3, v14
	v_exp_f32_e32 v2, v2
	v_exp_f32_e32 v3, v3
	ds_read2_b32 v[12:13], v236 offset0:192 offset1:224
	v_sub_f32_e32 v6, v6, v14
	v_sub_f32_e32 v7, v7, v14
	v_pk_mul_f32 v[18:19], v[10:11], v[4:5]
	v_sub_f32_e32 v4, v247, v14
	ds_read2_b32 v[22:23], v165 offset0:64 offset1:96
	ds_read2_b32 v[24:25], v165 offset0:128 offset1:160
	ds_read2_b32 v[26:27], v165 offset0:192 offset1:224
	v_exp_f32_e32 v6, v6
	v_exp_f32_e32 v7, v7
	v_exp_f32_e32 v34, v4
	v_max_f32_e32 v4, v17, v17
	v_max_f32_e32 v5, v16, v16
	v_add_f32_e32 v0, 0, v0
	s_waitcnt lgkmcnt(4)
	v_pk_mul_f32 v[2:3], v[8:9], v[2:3]
	v_max_f32_e32 v4, v5, v4
	v_add_f32_e32 v0, v0, v1
	s_waitcnt lgkmcnt(2)
	v_max3_f32 v4, v4, v22, v23
	v_add_f32_e32 v0, v0, v2
	s_waitcnt lgkmcnt(1)
	v_max3_f32 v4, v4, v24, v25
	v_add_f32_e32 v0, v0, v3
	v_pk_mul_f32 v[20:21], v[12:13], v[6:7]
	s_waitcnt lgkmcnt(0)
	v_max3_f32 v35, v4, v26, v27
	v_add_f32_e32 v18, v0, v18
	ds_read_b128 v[0:3], v245
	ds_read_b128 v[4:7], v237
	v_sub_f32_e32 v8, v16, v35
	v_exp_f32_e32 v16, v8
	ds_read2_b32 v[28:29], v242 offset1:32
	ds_read_b128 v[8:11], v245 offset:34816
	ds_read_b128 v[12:15], v245 offset:60928
	s_min_u32 s57, s57, 5
	s_waitcnt lgkmcnt(3)
	v_pk_add_f32 v[0:1], v[0:1], v[4:5]
	v_pk_add_f32 v[2:3], v[2:3], v[6:7]
	v_pk_fma_f32 v[30:31], v[16:17], v[0:1], 0 op_sel_hi:[0,1,0]
	v_sub_f32_e32 v0, v17, v35
	v_pk_fma_f32 v[32:33], v[16:17], v[2:3], 0 op_sel_hi:[0,1,0]
	v_exp_f32_e32 v17, v0
	v_add_f32_e32 v0, v18, v19
	v_add_f32_e32 v0, v0, v20
	v_add_f32_e32 v36, v0, v21
	ds_read_b128 v[0:3], v245 offset:8704
	ds_read_b128 v[4:7], v245 offset:17408
	s_waitcnt lgkmcnt(4)
	v_pk_mul_f32 v[18:19], v[28:29], v[16:17]
	v_sub_f32_e32 v16, v22, v35
	v_exp_f32_e32 v16, v16
	v_add_f32_e32 v20, 0, v18
	v_mov_b32_e32 v18, v17
	s_waitcnt lgkmcnt(1)
	v_pk_fma_f32 v[0:1], v[18:19], v[0:1], v[30:31] op_sel_hi:[0,1,1]
	v_pk_fma_f32 v[2:3], v[18:19], v[2:3], v[32:33] op_sel_hi:[0,1,1]
	s_waitcnt lgkmcnt(0)
	v_pk_fma_f32 v[4:5], v[16:17], v[4:5], v[0:1] op_sel_hi:[0,1,1]
	v_sub_f32_e32 v0, v23, v35
	v_pk_fma_f32 v[6:7], v[16:17], v[6:7], v[2:3] op_sel_hi:[0,1,1]
	v_exp_f32_e32 v17, v0
	v_add_f32_e32 v21, v20, v19
	ds_read_b128 v[0:3], v245 offset:26112
	ds_read2_b32 v[18:19], v242 offset0:64 offset1:96
	v_sub_f32_e32 v22, v24, v35
	v_exp_f32_e32 v22, v22
	v_mov_b32_e32 v20, v17
	s_waitcnt lgkmcnt(1)
	v_pk_fma_f32 v[0:1], v[20:21], v[0:1], v[4:5] op_sel_hi:[0,1,1]
	v_pk_fma_f32 v[2:3], v[20:21], v[2:3], v[6:7] op_sel_hi:[0,1,1]
	ds_read2_b32 v[4:5], v242 offset0:128 offset1:160
	v_pk_fma_f32 v[8:9], v[22:23], v[8:9], v[0:1] op_sel_hi:[0,1,1]
	v_sub_f32_e32 v0, v25, v35
	v_pk_fma_f32 v[10:11], v[22:23], v[10:11], v[2:3] op_sel_hi:[0,1,1]
	v_exp_f32_e32 v23, v0
	s_waitcnt lgkmcnt(1)
	v_pk_mul_f32 v[0:1], v[18:19], v[16:17]
	s_lshl_b32 s58, s58, 18
	v_add_f32_e32 v0, v21, v0
	v_add_f32_e32 v2, v0, v1
	s_waitcnt lgkmcnt(0)
	v_pk_mul_f32 v[0:1], v[4:5], v[22:23]
	v_sub_f32_e32 v4, v26, v35
	v_add_f32_e32 v0, v2, v0
	v_add_f32_e32 v17, v0, v1
	ds_read_b128 v[0:3], v245 offset:43520
	v_exp_f32_e32 v18, v4
	ds_read2_b32 v[20:21], v242 offset0:192 offset1:224
	v_sub_f32_e32 v4, v27, v35
	v_exp_f32_e32 v19, v4
	ds_read_b128 v[4:7], v245 offset:52224
	v_mov_b32_e32 v16, v23
	s_waitcnt lgkmcnt(2)
	v_pk_fma_f32 v[0:1], v[16:17], v[0:1], v[8:9] op_sel_hi:[0,1,1]
	s_waitcnt lgkmcnt(1)
	v_pk_mul_f32 v[8:9], v[20:21], v[18:19]
	v_pk_fma_f32 v[2:3], v[16:17], v[2:3], v[10:11] op_sel_hi:[0,1,1]
	v_add_f32_e32 v8, v17, v8
	v_add_f32_e32 v8, v8, v9
	s_waitcnt lgkmcnt(0)
	v_pk_fma_f32 v[0:1], v[18:19], v[4:5], v[0:1] op_sel_hi:[0,1,1]
	v_div_scale_f32 v5, s[60:61], v8, v8, 1.0
	v_pk_fma_f32 v[2:3], v[18:19], v[6:7], v[2:3] op_sel_hi:[0,1,1]
	v_rcp_f32_e32 v6, v5
	v_mov_b32_e32 v4, v19
	v_pk_fma_f32 v[2:3], v[4:5], v[14:15], v[2:3] op_sel_hi:[0,1,1]
	v_pk_fma_f32 v[0:1], v[4:5], v[12:13], v[0:1] op_sel_hi:[0,1,1]
	v_fma_f32 v4, -v5, v6, 1.0
	v_fmac_f32_e32 v6, v4, v6
	v_div_scale_f32 v4, vcc, 1.0, v8, 1.0
	v_mul_f32_e32 v7, v4, v6
	v_fma_f32 v9, -v5, v7, v4
	v_fmac_f32_e32 v7, v9, v6
	v_fma_f32 v4, -v5, v7, v4
	v_div_fmas_f32 v4, v4, v6, v7
	s_lshl_b32 s60, s56, 19
	s_lshl_b32 s61, s55, 13
	v_div_fixup_f32 v4, v4, v8, 1.0
	s_add_i32 s60, s60, s61
	v_pk_mul_f32 v[2:3], v[2:3], v[4:5] op_sel_hi:[1,0]
	v_pk_mul_f32 v[0:1], v[0:1], v[4:5] op_sel_hi:[1,0]
	v_or_b32_e32 v4, s60, v230
	s_lshl_b32 s60, s57, 2
	s_add_i32 s60, s60, 8
	s_and_b32 s60, s60, 56
	s_and_b32 s57, s57, 1
	s_or_b32 s60, s60, s27
	s_or_b32 s57, s57, s28
	s_lshl_b32 s60, s60, 19
	s_lshl_b32 s57, s57, 13
	s_add_i32 s60, s60, s57
	s_or_b32 s62, s39, s59
	s_lshl_b32 s62, s62, 12
	global_store_dwordx4 v4, v[0:3], s[8:9] nt
	v_mov_b32_e32 v252, v34
	v_mov_b32_e32 v253, v36
	v_or_b32_e32 v0, s60, v230
	s_barrier
	global_load_dwordx4 v[128:131], v0, s[4:5]
	s_add_i32 s63, s62, 0x4000
	s_and_b32 s63, s63, 0x3f000
	s_or_b32 s63, s63, s58
	v_or_b32_e32 v2, s63, v231
	global_load_dwordx4 v[32:35], v2, s[6:7]
	global_load_dwordx4 v[36:39], v2, s[6:7] offset:1024
	s_add_i32 s63, s62, 0x5000
	s_and_b32 s63, s63, 0x3f000
	s_or_b32 s63, s63, s58
	v_or_b32_e32 v3, s63, v231
	global_load_dwordx4 v[16:19], v3, s[6:7]
	global_load_dwordx4 v[20:23], v3, s[6:7] offset:1024
	global_load_dwordx4 v[24:27], v3, s[6:7] offset:2048
	global_load_dwordx4 v[28:31], v3, s[6:7] offset:3072
	s_add_i32 s63, s62, 0x6000
	s_and_b32 s63, s63, 0x3f000
	s_or_b32 s63, s63, s58
	v_or_b32_e32 v2, s63, v231
	global_load_dwordx4 v[4:7], v2, s[6:7]
	global_load_dwordx4 v[8:11], v2, s[6:7] offset:1024
	global_load_dwordx4 v[12:15], v2, s[6:7] offset:2048
	v_div_scale_f32 v1, s[64:65], v253, v253, v252
	v_rcp_f32_e32 v2, v1
	s_nop 0
	v_fma_f32 v0, -v1, v2, 1.0
	v_fmac_f32_e32 v2, v0, v2
	v_div_scale_f32 v0, vcc, v252, v253, v252
	v_mul_f32_e32 v3, v0, v2
	v_fma_f32 v248, -v1, v3, v0
	v_fmac_f32_e32 v3, v248, v2
	v_fma_f32 v0, -v1, v3, v0
	v_div_fmas_f32 v0, v0, v2, v3
	v_div_fixup_f32 v1, v0, v253, v252
	v_mul_f32_e32 v0, s18, v1
	v_mov_b32_e32 v2, s26
	v_mov_b32_e32 v3, s23
	v_cmp_eq_u32_e64 s[64:65], 0, v233
	v_cmp_eq_u32_e64 s[66:67], 1, v233
	v_cmp_eq_u32_e64 s[68:69], 2, v233
	v_cmp_eq_u32_e64 s[70:71], 3, v233
	v_cndmask_b32_e64 v248, v2, v3, s[64:65]
	v_cndmask_b32_e64 v249, v2, v3, s[66:67]
	v_cndmask_b32_e64 v250, v2, v3, s[68:69]
	v_cndmask_b32_e64 v251, v2, v3, s[70:71]
	v_mul_f32_e32 v248, v1, v248
	v_mul_f32_e32 v249, v1, v249
	v_mul_f32_e32 v250, v1, v250
	v_mul_f32_e32 v251, v1, v251
	v_cndmask_b32_e64 v248, v0, v248, s[2:3]
	v_cndmask_b32_e64 v249, v0, v249, s[2:3]
	v_cndmask_b32_e64 v250, v0, v250, s[2:3]
	v_cndmask_b32_e64 v251, v0, v251, s[2:3]
	v_mul_f32_e32 v248, v248, v208
	v_mul_f32_e32 v249, v249, v209
	v_mul_f32_e32 v250, v250, v204
	v_mul_f32_e32 v251, v251, v205
	ds_write_b128 v238, v[248:251]
	v_cmp_eq_u32_e64 s[64:65], 4, v233
	v_cmp_eq_u32_e64 s[66:67], 5, v233
	v_cmp_eq_u32_e64 s[68:69], 6, v233
	v_cmp_eq_u32_e64 s[70:71], 7, v233
	v_cndmask_b32_e64 v248, v2, v3, s[64:65]
	v_cndmask_b32_e64 v249, v2, v3, s[66:67]
	v_cndmask_b32_e64 v250, v2, v3, s[68:69]
	v_cndmask_b32_e64 v251, v2, v3, s[70:71]
	v_mul_f32_e32 v248, v1, v248
	v_mul_f32_e32 v249, v1, v249
	v_mul_f32_e32 v250, v1, v250
	v_mul_f32_e32 v251, v1, v251
	v_cndmask_b32_e64 v248, v0, v248, s[2:3]
	v_cndmask_b32_e64 v249, v0, v249, s[2:3]
	v_cndmask_b32_e64 v250, v0, v250, s[2:3]
	v_cndmask_b32_e64 v251, v0, v251, s[2:3]
	v_mul_f32_e32 v248, v248, v182
	v_mul_f32_e32 v249, v249, v183
	v_mul_f32_e32 v250, v250, v178
	v_mul_f32_e32 v251, v251, v179
	ds_write_b128 v238, v[248:251] offset:32
	v_cmp_eq_u32_e64 s[64:65], 8, v233
	v_cmp_eq_u32_e64 s[66:67], 9, v233
	v_cmp_eq_u32_e64 s[68:69], 10, v233
	v_cmp_eq_u32_e64 s[70:71], 11, v233
	v_cndmask_b32_e64 v248, v2, v3, s[64:65]
	v_cndmask_b32_e64 v249, v2, v3, s[66:67]
	v_cndmask_b32_e64 v250, v2, v3, s[68:69]
	v_cndmask_b32_e64 v251, v2, v3, s[70:71]
	v_mul_f32_e32 v248, v1, v248
	v_mul_f32_e32 v249, v1, v249
	v_mul_f32_e32 v250, v1, v250
	v_mul_f32_e32 v251, v1, v251
	v_cndmask_b32_e64 v248, v0, v248, s[2:3]
	v_cndmask_b32_e64 v249, v0, v249, s[2:3]
	v_cndmask_b32_e64 v250, v0, v250, s[2:3]
	v_cndmask_b32_e64 v251, v0, v251, s[2:3]
	v_mul_f32_e32 v248, v248, v166
	v_mul_f32_e32 v249, v249, v167
	v_mul_f32_e32 v250, v250, v118
	v_mul_f32_e32 v251, v251, v119
	ds_write_b128 v238, v[248:251] offset:64
	v_cmp_eq_u32_e64 s[64:65], 12, v233
	v_cmp_eq_u32_e64 s[66:67], 13, v233
	v_cmp_eq_u32_e64 s[68:69], 14, v233
	v_cmp_eq_u32_e64 s[70:71], 15, v233
	v_cndmask_b32_e64 v248, v2, v3, s[64:65]
	v_cndmask_b32_e64 v249, v2, v3, s[66:67]
	v_cndmask_b32_e64 v250, v2, v3, s[68:69]
	v_cndmask_b32_e64 v251, v2, v3, s[70:71]
	v_mul_f32_e32 v248, v1, v248
	v_mul_f32_e32 v249, v1, v249
	v_mul_f32_e32 v250, v1, v250
	v_mul_f32_e32 v251, v1, v251
	v_cndmask_b32_e64 v248, v0, v248, s[2:3]
	v_cndmask_b32_e64 v249, v0, v249, s[2:3]
	v_cndmask_b32_e64 v250, v0, v250, s[2:3]
	v_cndmask_b32_e64 v251, v0, v251, s[2:3]
	v_mul_f32_e32 v248, v248, v116
	v_mul_f32_e32 v249, v249, v117
	v_mul_f32_e32 v250, v250, v114
	v_mul_f32_e32 v251, v251, v115
	ds_write_b128 v238, v[248:251] offset:96
	v_pk_mul_f32 v[248:249], v[0:1], v[112:113] op_sel_hi:[0,1]
	v_pk_mul_f32 v[250:251], v[0:1], v[98:99] op_sel_hi:[0,1]
	ds_write_b128 v238, v[248:251] offset:128
	v_pk_mul_f32 v[248:249], v[0:1], v[100:101] op_sel_hi:[0,1]
	v_pk_mul_f32 v[250:251], v[0:1], v[120:121] op_sel_hi:[0,1]
	ds_write_b128 v238, v[248:251] offset:160
	v_pk_mul_f32 v[248:249], v[0:1], v[102:103] op_sel_hi:[0,1]
	v_pk_mul_f32 v[250:251], v[0:1], v[122:123] op_sel_hi:[0,1]
	ds_write_b128 v238, v[248:251] offset:192
	v_pk_mul_f32 v[248:249], v[0:1], v[124:125] op_sel_hi:[0,1]
	v_pk_mul_f32 v[250:251], v[0:1], v[180:181] op_sel_hi:[0,1]
	ds_write_b128 v238, v[248:251] offset:224
	s_lshl_b32 s56, s56, 11
	s_add_i32 s56, s56, s25
	v_or_b32_e32 v252, s56, v239
	v_add_lshl_u32 v253, v241, s55, 7
	v_lshl_or_b32 v1, v252, 13, v240
	v_and_or_b32 v2, v253, s54, v1
	ds_read_b128 v[248:251], v246
	ds_read_b128 v[160:163], v246 offset:1088
	s_waitcnt lgkmcnt(1)
	global_store_dwordx4 v2, v[248:251], s[10:11] sc0 nt
	s_nop 0
	ds_read_b128 v[248:251], v246 offset:2176
	v_or_b32_e32 v3, 0x8000, v2
	s_waitcnt lgkmcnt(1)
	global_store_dwordx4 v3, v[160:163], s[10:11] sc0 nt
	s_nop 0
	ds_read_b128 v[160:163], v246 offset:3264
	v_or_b32_e32 v252, 0x10000, v2
	s_waitcnt lgkmcnt(1)
	global_store_dwordx4 v252, v[248:251], s[10:11] sc0 nt
	s_nop 0
	ds_read_b128 v[248:251], v246 offset:4352
	v_or_b32_e32 v3, 0x18000, v2
	s_waitcnt lgkmcnt(1)
	global_store_dwordx4 v3, v[160:163], s[10:11] sc0 nt
	s_nop 0
	ds_read_b128 v[160:163], v246 offset:5440
	v_or_b32_e32 v252, 0x20000, v2
	s_waitcnt lgkmcnt(1)
	global_store_dwordx4 v252, v[248:251], s[10:11] sc0 nt
	s_nop 0
	ds_read_b128 v[248:251], v246 offset:6528
	v_or_b32_e32 v3, 0x28000, v2
	s_waitcnt lgkmcnt(1)
	global_store_dwordx4 v3, v[160:163], s[10:11] sc0 nt
	s_nop 0
	ds_read_b128 v[160:163], v246 offset:7616
	v_or_b32_e32 v252, 0x30000, v2
	s_waitcnt lgkmcnt(1)
	global_store_dwordx4 v252, v[248:251], s[10:11] sc0 nt
	v_or_b32_e32 v3, 0x38000, v2
	s_waitcnt lgkmcnt(0)
	global_store_dwordx4 v3, v[160:163], s[10:11] sc0 nt
	v_pk_mul_f32 v[248:249], v[0:1], v[80:81] op_sel_hi:[0,1]
	v_pk_mul_f32 v[250:251], v[0:1], v[82:83] op_sel_hi:[0,1]
	ds_write_b128 v238, v[248:251]
	v_pk_mul_f32 v[248:249], v[0:1], v[84:85] op_sel_hi:[0,1]
	v_pk_mul_f32 v[250:251], v[0:1], v[96:97] op_sel_hi:[0,1]
	ds_write_b128 v238, v[248:251] offset:32
	v_pk_mul_f32 v[248:249], v[0:1], v[86:87] op_sel_hi:[0,1]
	v_pk_mul_f32 v[250:251], v[0:1], v[88:89] op_sel_hi:[0,1]
	ds_write_b128 v238, v[248:251] offset:64
	v_pk_mul_f32 v[248:249], v[0:1], v[90:91] op_sel_hi:[0,1]
	v_pk_mul_f32 v[250:251], v[0:1], v[94:95] op_sel_hi:[0,1]
	ds_write_b128 v238, v[248:251] offset:96
	v_pk_mul_f32 v[248:249], v[0:1], v[92:93] op_sel_hi:[0,1]
	v_pk_mul_f32 v[250:251], v[0:1], v[108:109] op_sel_hi:[0,1]
	ds_write_b128 v238, v[248:251] offset:128
	v_pk_mul_f32 v[248:249], v[0:1], v[110:111] op_sel_hi:[0,1]
	v_pk_mul_f32 v[250:251], v[0:1], v[176:177] op_sel_hi:[0,1]
	ds_write_b128 v238, v[248:251] offset:160
	v_pk_mul_f32 v[248:249], v[0:1], v[174:175] op_sel_hi:[0,1]
	v_pk_mul_f32 v[250:251], v[0:1], v[192:193] op_sel_hi:[0,1]
	ds_write_b128 v238, v[248:251] offset:192
	v_pk_mul_f32 v[248:249], v[0:1], v[194:195] op_sel_hi:[0,1]
	v_pk_mul_f32 v[250:251], v[0:1], v[206:207] op_sel_hi:[0,1]
	ds_write_b128 v238, v[248:251] offset:224
	v_add_u32_e32 v252, 0x100, v253
	v_and_or_b32 v2, v252, s54, v1
	ds_read_b128 v[248:251], v246
	ds_read_b128 v[160:163], v246 offset:1088
	s_waitcnt lgkmcnt(1)
	global_store_dwordx4 v2, v[248:251], s[10:11] sc0 nt
	s_nop 0
	ds_read_b128 v[248:251], v246 offset:2176
	v_or_b32_e32 v3, 0x8000, v2
	s_waitcnt lgkmcnt(1)
	global_store_dwordx4 v3, v[160:163], s[10:11] sc0 nt
	s_nop 0
	ds_read_b128 v[160:163], v246 offset:3264
	v_or_b32_e32 v252, 0x10000, v2
	s_waitcnt lgkmcnt(1)
	global_store_dwordx4 v252, v[248:251], s[10:11] sc0 nt
	s_nop 0
	ds_read_b128 v[248:251], v246 offset:4352
	v_or_b32_e32 v3, 0x18000, v2
	s_waitcnt lgkmcnt(1)
	global_store_dwordx4 v3, v[160:163], s[10:11] sc0 nt
	s_nop 0
	ds_read_b128 v[160:163], v246 offset:5440
	v_or_b32_e32 v252, 0x20000, v2
	s_waitcnt lgkmcnt(1)
	global_store_dwordx4 v252, v[248:251], s[10:11] sc0 nt
	s_nop 0
	ds_read_b128 v[248:251], v246 offset:6528
	v_or_b32_e32 v3, 0x28000, v2
	s_waitcnt lgkmcnt(1)
	global_store_dwordx4 v3, v[160:163], s[10:11] sc0 nt
	s_nop 0
	ds_read_b128 v[160:163], v246 offset:7616
	v_or_b32_e32 v252, 0x30000, v2
	s_waitcnt lgkmcnt(1)
	global_store_dwordx4 v252, v[248:251], s[10:11] sc0 nt
	v_or_b32_e32 v3, 0x38000, v2
	s_waitcnt lgkmcnt(0)
	global_store_dwordx4 v3, v[160:163], s[10:11] sc0 nt
	s_add_i32 s63, s62, 0x3000
	s_and_b32 s63, s63, 0x3f000
	s_or_b32 s63, s63, s58
	v_or_b32_e32 v2, s63, v231
	global_load_dwordx4 v[80:83], v2, s[6:7]
	global_load_dwordx4 v[84:87], v2, s[6:7] offset:1024
	global_load_dwordx4 v[88:91], v2, s[6:7] offset:2048
	global_load_dwordx4 v[92:95], v2, s[6:7] offset:3072
	s_add_i32 s63, s62, 0x2000
	s_and_b32 s63, s63, 0x3f000
	s_or_b32 s63, s63, s58
	v_or_b32_e32 v3, s63, v231
	global_load_dwordx4 v[96:99], v3, s[6:7]
	global_load_dwordx4 v[100:103], v3, s[6:7] offset:1024
	global_load_dwordx4 v[108:111], v3, s[6:7] offset:2048
	global_load_dwordx4 v[192:195], v3, s[6:7] offset:3072
	s_add_i32 s63, s62, 0x1000
	s_and_b32 s63, s63, 0x3f000
	s_or_b32 s63, s63, s58
	v_or_b32_e32 v2, s63, v231
	global_load_dwordx4 v[174:177], v2, s[6:7] offset:2048
	global_load_dwordx4 v[178:181], v2, s[6:7] offset:3072
	v_pk_mul_f32 v[248:249], v[0:1], v[64:65] op_sel_hi:[0,1]
	v_pk_mul_f32 v[250:251], v[0:1], v[66:67] op_sel_hi:[0,1]
	ds_write_b128 v238, v[248:251]
	v_pk_mul_f32 v[248:249], v[0:1], v[68:69] op_sel_hi:[0,1]
	v_pk_mul_f32 v[250:251], v[0:1], v[74:75] op_sel_hi:[0,1]
	ds_write_b128 v238, v[248:251] offset:32
	v_pk_mul_f32 v[248:249], v[0:1], v[72:73] op_sel_hi:[0,1]
	v_pk_mul_f32 v[250:251], v[0:1], v[104:105] op_sel_hi:[0,1]
	ds_write_b128 v238, v[248:251] offset:64
	v_pk_mul_f32 v[248:249], v[0:1], v[106:107] op_sel_hi:[0,1]
	v_pk_mul_f32 v[250:251], v[0:1], v[172:173] op_sel_hi:[0,1]
	ds_write_b128 v238, v[248:251] offset:96
	v_pk_mul_f32 v[248:249], v[0:1], v[170:171] op_sel_hi:[0,1]
	v_pk_mul_f32 v[250:251], v[0:1], v[188:189] op_sel_hi:[0,1]
	ds_write_b128 v238, v[248:251] offset:128
	v_pk_mul_f32 v[248:249], v[0:1], v[190:191] op_sel_hi:[0,1]
	v_pk_mul_f32 v[250:251], v[0:1], v[202:203] op_sel_hi:[0,1]
	ds_write_b128 v238, v[248:251] offset:160
	v_pk_mul_f32 v[248:249], v[0:1], v[200:201] op_sel_hi:[0,1]
	v_pk_mul_f32 v[250:251], v[0:1], v[214:215] op_sel_hi:[0,1]
	ds_write_b128 v238, v[248:251] offset:192
	v_pk_mul_f32 v[248:249], v[0:1], v[216:217] op_sel_hi:[0,1]
	v_pk_mul_f32 v[250:251], v[0:1], v[222:223] op_sel_hi:[0,1]
	ds_write_b128 v238, v[248:251] offset:224
	v_add_u32_e32 v252, 0x200, v253
	v_and_or_b32 v2, v252, s54, v1
	ds_read_b128 v[248:251], v246
	ds_read_b128 v[160:163], v246 offset:1088
	s_waitcnt lgkmcnt(1)
	global_store_dwordx4 v2, v[248:251], s[10:11] sc0 nt
	s_nop 0
	ds_read_b128 v[248:251], v246 offset:2176
	v_or_b32_e32 v3, 0x8000, v2
	s_waitcnt lgkmcnt(1)
	global_store_dwordx4 v3, v[160:163], s[10:11] sc0 nt
	s_nop 0
	ds_read_b128 v[160:163], v246 offset:3264
	v_or_b32_e32 v252, 0x10000, v2
	s_waitcnt lgkmcnt(1)
	global_store_dwordx4 v252, v[248:251], s[10:11] sc0 nt
	s_nop 0
	ds_read_b128 v[248:251], v246 offset:4352
	v_or_b32_e32 v3, 0x18000, v2
	s_waitcnt lgkmcnt(1)
	global_store_dwordx4 v3, v[160:163], s[10:11] sc0 nt
	s_nop 0
	ds_read_b128 v[160:163], v246 offset:5440
	v_or_b32_e32 v252, 0x20000, v2
	s_waitcnt lgkmcnt(1)
	global_store_dwordx4 v252, v[248:251], s[10:11] sc0 nt
	s_nop 0
	ds_read_b128 v[248:251], v246 offset:6528
	v_or_b32_e32 v3, 0x28000, v2
	s_waitcnt lgkmcnt(1)
	global_store_dwordx4 v3, v[160:163], s[10:11] sc0 nt
	s_nop 0
	ds_read_b128 v[160:163], v246 offset:7616
	v_or_b32_e32 v252, 0x30000, v2
	s_waitcnt lgkmcnt(1)
	global_store_dwordx4 v252, v[248:251], s[10:11] sc0 nt
	v_or_b32_e32 v3, 0x38000, v2
	s_waitcnt lgkmcnt(0)
	global_store_dwordx4 v3, v[160:163], s[10:11] sc0 nt
	v_pk_mul_f32 v[248:249], v[0:1], v[70:71] op_sel_hi:[0,1]
	v_pk_mul_f32 v[250:251], v[0:1], v[76:77] op_sel_hi:[0,1]
	ds_write_b128 v238, v[248:251]
	v_pk_mul_f32 v[248:249], v[0:1], v[78:79] op_sel_hi:[0,1]
	v_pk_mul_f32 v[250:251], v[0:1], v[168:169] op_sel_hi:[0,1]
	ds_write_b128 v238, v[248:251] offset:32
	v_pk_mul_f32 v[248:249], v[0:1], v[126:127] op_sel_hi:[0,1]
	v_pk_mul_f32 v[250:251], v[0:1], v[184:185] op_sel_hi:[0,1]
	ds_write_b128 v238, v[248:251] offset:64
	v_pk_mul_f32 v[248:249], v[0:1], v[186:187] op_sel_hi:[0,1]
	v_pk_mul_f32 v[250:251], v[0:1], v[198:199] op_sel_hi:[0,1]
	ds_write_b128 v238, v[248:251] offset:96
	v_pk_mul_f32 v[248:249], v[0:1], v[196:197] op_sel_hi:[0,1]
	v_pk_mul_f32 v[250:251], v[0:1], v[210:211] op_sel_hi:[0,1]
	ds_write_b128 v238, v[248:251] offset:128
	v_pk_mul_f32 v[248:249], v[0:1], v[212:213] op_sel_hi:[0,1]
	v_pk_mul_f32 v[250:251], v[0:1], v[220:221] op_sel_hi:[0,1]
	ds_write_b128 v238, v[248:251] offset:160
	v_pk_mul_f32 v[248:249], v[0:1], v[218:219] op_sel_hi:[0,1]
	v_pk_mul_f32 v[250:251], v[0:1], v[224:225] op_sel_hi:[0,1]
	ds_write_b128 v238, v[248:251] offset:192
	v_pk_mul_f32 v[248:249], v[0:1], v[226:227] op_sel_hi:[0,1]
	v_pk_mul_f32 v[250:251], v[0:1], v[228:229] op_sel_hi:[0,1]
	ds_write_b128 v238, v[248:251] offset:224
	v_add_u32_e32 v252, 0x300, v253
	v_and_or_b32 v196, v252, s54, v1
	s_mov_b32 s72, s55
	s_mov_b32 s73, s56
	s_cmp_lt_u32 s31, 0x200
	s_cbranch_scc1 .Ltail_end
	s_waitcnt lgkmcnt(0)
	s_add_i32 s75, s12, 4
	v_mov_b32_e32 v248, s74
	v_mov_b32_e32 v249, s75
	ds_write_b32 v248, v249

.LBB1_22:
	ds_read_b128 v[184:187], v246
	ds_read_b128 v[188:191], v246 offset:1088
	s_waitcnt lgkmcnt(1)
	global_store_dwordx4 v196, v[184:187], s[10:11] sc0 nt
	s_nop 0
	ds_read_b128 v[184:187], v246 offset:2176
	v_or_b32_e32 v197, 0x8000, v196
	s_waitcnt lgkmcnt(1)
	global_store_dwordx4 v197, v[188:191], s[10:11] sc0 nt
	s_nop 0
	ds_read_b128 v[188:191], v246 offset:3264
	v_or_b32_e32 v197, 0x10000, v196
	s_waitcnt lgkmcnt(1)
	global_store_dwordx4 v197, v[184:187], s[10:11] sc0 nt
	s_nop 0
	ds_read_b128 v[184:187], v246 offset:4352
	v_or_b32_e32 v197, 0x18000, v196
	s_waitcnt lgkmcnt(1)
	global_store_dwordx4 v197, v[188:191], s[10:11] sc0 nt
	s_nop 0
	ds_read_b128 v[188:191], v246 offset:5440
	v_or_b32_e32 v197, 0x20000, v196
	s_waitcnt lgkmcnt(1)
	global_store_dwordx4 v197, v[184:187], s[10:11] sc0 nt
	s_nop 0
	ds_read_b128 v[184:187], v246 offset:6528
	v_or_b32_e32 v197, 0x28000, v196
	s_waitcnt lgkmcnt(1)
	global_store_dwordx4 v197, v[188:191], s[10:11] sc0 nt
	s_nop 0
	ds_read_b128 v[188:191], v246 offset:7616
	v_or_b32_e32 v197, 0x30000, v196
	s_waitcnt lgkmcnt(1)
	global_store_dwordx4 v197, v[184:187], s[10:11] sc0 nt
	v_or_b32_e32 v197, 0x38000, v196
	s_waitcnt lgkmcnt(0)
	global_store_dwordx4 v197, v[188:191], s[10:11] sc0 nt
